# speedup vs baseline: 1.0365x; 1.0365x over previous
_Z6k_gemmPKfS0_PK15HIP_vector_typeIjLj4EEPDF16_PKh:
	s_load_dwordx4 s[20:23], s[0:1], 0x0
	s_load_dwordx4 s[4:7], s[0:1], 0x10
	s_load_dwordx2 s[38:39], s[0:1], 0x20
	v_readfirstlane_b32 s8, v0
	v_and_b32_e32 v1, 63, v0
	s_nop 3
	s_lshr_b32 s8, s8, 6
	s_and_b32 s40, s2, 7
	s_lshr_b32 s41, s2, 3
	s_mul_i32 s18, s40, 0x187
	s_min_u32 s19, s18, 0xaae
	s_add_i32 s18, s18, s41
	s_sub_i32 s33, s19, s18
	s_addk_i32 s33, 0x1c6
	s_ashr_i32 s9, s33, 6
	s_max_i32 s9, s9, 0
	s_cmp_eq_u32 s9, 0
	s_cbranch_scc1 .Lg_end
	s_add_i32 s11, s9, 4
	s_lshl_b32 s18, s18, 4
	s_lshl_b32 s19, s8, 2
	s_add_i32 s33, s18, s19
	s_mul_i32 s12, s33, 0x4b0
	s_lshl_b32 s32, s18, 8
	s_sub_u32 s32, s32, 0x100000
	s_mov_b32 s10, 0
	v_lshl_add_u32 v253, v1, 10, s33
	v_mov_b32_e32 v247, 0
	v_cmp_gt_i32_e32 vcc, s9, v1
	s_mov_b32 s18, 0xc350
	v_cmp_gt_i32_e64 s[36:37], s18, v253
	s_and_b64 vcc, vcc, s[36:37]
	s_waitcnt lgkmcnt(0)
	s_and_saveexec_b64 s[36:37], vcc
	global_load_dword v247, v253, s[38:39]
	s_mov_b64 exec, s[36:37]
	s_mov_b32 s24, s22
	s_and_b32 s25, s23, 0xffff
	s_mov_b32 s26, 0x3938700
	s_mov_b32 s27, 0x20000
	s_and_b32 s21, s21, 0xffff
	s_mov_b32 s22, 0x3938700
	s_mov_b32 s23, 0x20000
	s_mov_b32 s28, s6
	s_and_b32 s29, s7, 0xffff
	s_mov_b32 s30, 0xc35000
	s_mov_b32 s31, 0x20000
	v_lshlrev_b32_e32 v238, 4, v1
	v_mul_u32_u24_e32 v253, 0x1746, v1
	v_lshrrev_b32_e32 v253, 16, v253
	v_min_u32_e32 v253, 3, v253
	v_mul_u32_u24_e32 v254, 11, v253
	v_sub_u32_e32 v254, v1, v254
	v_lshlrev_b32_e32 v240, 3, v253
	v_mul_u32_u24_e32 v249, 0x4b0, v253
	v_lshl_add_u32 v249, v254, 4, v249
	v_add_u32_e32 v249, 0x400, v249
	v_mov_b32_e32 v255, 0x80000000
	v_cmp_gt_u32_e64 s[34:35], 44, v1
	s_nop 1
	v_cndmask_b32_e64 v239, v255, v249, s[34:35]
	v_lshl_add_u32 v250, s8, 2, v253
	v_mul_u32_u24_e32 v250, 0x4e0, v250
	v_lshl_add_u32 v250, v254, 3, v250
	v_add_u32_e32 v242, 0x200, v250
	s_mul_i32 s18, s8, 0x1380
	v_lshl_add_u32 v241, v1, 3, s18
	v_and_b32_e32 v249, 15, v1
	v_lshrrev_b32_e32 v250, 4, v1
	v_mul_u32_u24_e32 v243, 0x4e0, v249
	v_lshl_add_u32 v243, v250, 4, v243
	v_mul_u32_u24_e32 v244, 0x440, v250
	v_lshl_add_u32 v244, v249, 1, v244
	s_lshl_b32 s18, s8, 6
	s_add_i32 s18, s18, 39936
	v_add_u32_e32 v244, s18, v244
	v_lshrrev_b32_e32 v249, 4, v0
	v_and_b32_e32 v250, 15, v0
	v_mul_u32_u24_e32 v245, 0x110, v249
	v_lshl_add_u32 v245, v250, 4, v245
	v_add_u32_e32 v245, 39936, v245
	v_lshlrev_b32_e32 v246, 8, v249
	v_lshl_add_u32 v246, v250, 4, v246
	s_lshl_b32 s18, s8, 12
	s_add_i32 s18, s18, 48640
	v_lshl_add_u32 v248, v1, 4, s18
	v_cmp_gt_u32_e32 vcc, 32, v0
	s_and_saveexec_b64 s[36:37], vcc
	v_mul_u32_u24_e32 v251, 0x4e00, v249
	v_mul_u32_u24_e32 v252, 0x4e0, v250
	v_add_u32_e32 v254, v251, v252
	v_mov_b32_e32 v250, 0
	v_mov_b32_e32 v251, 0
	v_mov_b32_e32 v252, 0
	v_mov_b32_e32 v253, 0
	ds_write_b128 v254, v[250:253] offset:1200
	s_mov_b64 exec, s[36:37]
	s_lshl_b32 s18, s8, 11
	v_lshl_add_u32 v253, v1, 4, s18
	v_add_u32_e32 v254, 0x22000, v253
	global_load_dwordx4 v[178:181], v254, s[4:5]
	global_load_dwordx4 v[182:185], v254, s[4:5] offset:1024
	v_add_u32_e32 v254, 0x2000, v254
	global_load_dwordx4 v[186:189], v254, s[4:5]
	global_load_dwordx4 v[190:193], v254, s[4:5] offset:1024
	v_mov_b32_e32 v236, v253
	s_waitcnt vmcnt(4)
	v_readlane_b32 s13, v247, s10
	s_add_u32 s14, s12, 0x4b0
	s_add_u32 s15, s12, 0x960
	s_add_u32 s16, s12, 0xe10
	s_nop 1
	s_and_b32 s18, s13, 0xff
	s_cmp_eq_u32 s18, 1
	s_cselect_b32 s42, s12, 0x80000000
	s_and_b32 s18, s13, 0xff00
	s_cmp_eq_u32 s18, 0x100
	s_cselect_b32 s14, s14, 0x80000000
	s_and_b32 s18, s13, 0xff0000
	s_cmp_eq_u32 s18, 0x10000
	s_cselect_b32 s15, s15, 0x80000000
	s_and_b32 s18, s13, 0xff000000
	s_cmp_eq_u32 s18, 0x1000000
	s_cselect_b32 s16, s16, 0x80000000
	v_lshrrev_b32_e64 v253, v240, s13
	v_and_b32_e32 v253, 0xff, v253
	v_cmp_eq_u32_e32 vcc, 1, v253
	s_nop 1
	v_cndmask_b32_e32 v254, v255, v239, vcc
	buffer_load_dwordx4 v[138:141], v238, s[20:23], s42 offen nt
	buffer_load_dwordx4 v[142:145], v238, s[24:27], s42 offen nt
	buffer_load_dwordx4 v[146:149], v238, s[20:23], s14 offen nt
	buffer_load_dwordx4 v[150:153], v238, s[24:27], s14 offen nt
	buffer_load_dwordx4 v[154:157], v238, s[20:23], s15 offen nt
	buffer_load_dwordx4 v[158:161], v238, s[24:27], s15 offen nt
	buffer_load_dwordx4 v[162:165], v238, s[20:23], s16 offen nt
	buffer_load_dwordx4 v[166:169], v238, s[24:27], s16 offen nt
	buffer_load_dwordx4 v[170:173], v254, s[20:23], s12 offen nt
	buffer_load_dwordx4 v[174:177], v254, s[24:27], s12 offen nt
	s_add_u32 s12, s12, 0x12c000
	s_add_u32 s32, s32, 0x40000
	s_mov_b32 s10, 1
	global_load_dwordx4 v[2:5], v236, s[4:5]
	global_load_dwordx4 v[6:9], v236, s[4:5] offset:1024
	v_add_u32_e32 v236, 0x2000, v236
	global_load_dwordx4 v[10:13], v236, s[4:5]
	global_load_dwordx4 v[14:17], v236, s[4:5] offset:1024
	v_add_u32_e32 v236, 0x2000, v236
	global_load_dwordx4 v[18:21], v236, s[4:5]
	global_load_dwordx4 v[22:25], v236, s[4:5] offset:1024
	v_add_u32_e32 v236, 0x2000, v236
	global_load_dwordx4 v[26:29], v236, s[4:5]
	global_load_dwordx4 v[30:33], v236, s[4:5] offset:1024
	v_add_u32_e32 v236, 0x2000, v236
	global_load_dwordx4 v[34:37], v236, s[4:5]
	global_load_dwordx4 v[38:41], v236, s[4:5] offset:1024
	v_add_u32_e32 v236, 0x2000, v236
	global_load_dwordx4 v[42:45], v236, s[4:5]
	global_load_dwordx4 v[46:49], v236, s[4:5] offset:1024
	v_add_u32_e32 v236, 0x2000, v236
	global_load_dwordx4 v[50:53], v236, s[4:5]
	global_load_dwordx4 v[54:57], v236, s[4:5] offset:1024
	v_add_u32_e32 v236, 0x2000, v236
	global_load_dwordx4 v[58:61], v236, s[4:5]
	global_load_dwordx4 v[62:65], v236, s[4:5] offset:1024
	v_add_u32_e32 v236, 0x2000, v236
	global_load_dwordx4 v[66:69], v236, s[4:5]
	global_load_dwordx4 v[70:73], v236, s[4:5] offset:1024
	v_add_u32_e32 v236, 0x2000, v236
	global_load_dwordx4 v[74:77], v236, s[4:5]
	global_load_dwordx4 v[78:81], v236, s[4:5] offset:1024
	v_add_u32_e32 v236, 0x2000, v236
	global_load_dwordx4 v[82:85], v236, s[4:5]
	global_load_dwordx4 v[86:89], v236, s[4:5] offset:1024
	v_add_u32_e32 v236, 0x2000, v236
	global_load_dwordx4 v[90:93], v236, s[4:5]
	global_load_dwordx4 v[94:97], v236, s[4:5] offset:1024
	v_add_u32_e32 v236, 0x2000, v236
	global_load_dwordx4 v[98:101], v236, s[4:5]
	global_load_dwordx4 v[102:105], v236, s[4:5] offset:1024
	v_add_u32_e32 v236, 0x2000, v236
	global_load_dwordx4 v[106:109], v236, s[4:5]
	global_load_dwordx4 v[110:113], v236, s[4:5] offset:1024
	v_add_u32_e32 v236, 0x2000, v236
	global_load_dwordx4 v[114:117], v236, s[4:5]
	global_load_dwordx4 v[118:121], v236, s[4:5] offset:1024
	v_add_u32_e32 v236, 0x2000, v236
	global_load_dwordx4 v[122:125], v236, s[4:5]
	global_load_dwordx4 v[126:129], v236, s[4:5] offset:1024
	v_add_u32_e32 v236, 0x2000, v236
	global_load_dwordx4 v[130:133], v236, s[4:5]
	global_load_dwordx4 v[134:137], v236, s[4:5] offset:1024
	s_waitcnt vmcnt(44)
	ds_write_b128 v248, v[178:181]
	ds_write_b128 v248, v[182:185] offset:1024
	ds_write_b128 v248, v[186:189] offset:2048
	ds_write_b128 v248, v[190:193] offset:3072
	s_waitcnt lgkmcnt(0)
	s_barrier
	s_branch .Lg_half1

.Lg_half1:
	s_sub_u32 s18, s10, 2
	s_cmp_lt_u32 s18, s9
	s_cbranch_scc0 .Lg_s2skip1
	s_waitcnt vmcnt(21)
	v_cvt_pk_f16_f32 v250, v178, v179
	v_cvt_pk_f16_f32 v251, v180, v181
	ds_write_b64 v241, v[250:251] offset:19968
	s_waitcnt vmcnt(20)
	v_cvt_pk_f16_f32 v252, v182, v183
	v_cvt_pk_f16_f32 v253, v184, v185
	ds_write_b64 v241, v[252:253] offset:20568
	s_waitcnt vmcnt(19)
	v_cvt_pk_f16_f32 v250, v186, v187
	v_cvt_pk_f16_f32 v251, v188, v189
	ds_write_b64 v241, v[250:251] offset:21216
	s_waitcnt vmcnt(18)
	v_cvt_pk_f16_f32 v252, v190, v191
	v_cvt_pk_f16_f32 v253, v192, v193
	ds_write_b64 v241, v[252:253] offset:21816
	s_waitcnt vmcnt(17)
	v_cvt_pk_f16_f32 v250, v194, v195
	v_cvt_pk_f16_f32 v251, v196, v197
	ds_write_b64 v241, v[250:251] offset:22464
	s_waitcnt vmcnt(16)
	v_cvt_pk_f16_f32 v252, v198, v199
	v_cvt_pk_f16_f32 v253, v200, v201
	ds_write_b64 v241, v[252:253] offset:23064
	s_waitcnt vmcnt(15)
	v_cvt_pk_f16_f32 v250, v202, v203
	v_cvt_pk_f16_f32 v251, v204, v205
	ds_write_b64 v241, v[250:251] offset:23712
	s_waitcnt vmcnt(14)
	v_cvt_pk_f16_f32 v252, v206, v207
	v_cvt_pk_f16_f32 v253, v208, v209
	ds_write_b64 v241, v[252:253] offset:24312
	s_mov_b64 exec, s[34:35]
	s_waitcnt vmcnt(13)
	v_cvt_pk_f16_f32 v250, v210, v211
	v_cvt_pk_f16_f32 v251, v212, v213
	ds_write_b64 v242, v[250:251] offset:19968
	s_waitcnt vmcnt(12)
	v_cvt_pk_f16_f32 v252, v214, v215
	v_cvt_pk_f16_f32 v253, v216, v217
	ds_write_b64 v242, v[252:253] offset:20568
	s_mov_b64 exec, -1
